# MoE GEMM loops: the 64 readfirstlane waterfall loops around the LDS-DMA tile loads (scalar offsets that are the same in every lane) become readfirstlane + load; the second load of a pair reuses the sc
# speedup vs baseline: 1.0048x; 1.0048x over previous
.LBB0_1823:
	s_or_b64 exec, exec, s[4:5]
	s_add_u32 s54, s40, 0x10000
	s_addc_u32 s55, s41, 0
	s_add_u32 s24, s0, 0xf8
	s_addc_u32 s25, s1, 0
	s_add_i32 s4, 0, 0x20080
	v_mov_b32_e32 v1, s4
	s_waitcnt lgkmcnt(0)
	s_barrier
	ds_read_b32 v2, v1
	s_load_dword s33, s[0:1], 0xf8
	s_add_u32 s26, s40, 0x300000
	s_addc_u32 s27, s41, 0
	s_add_u32 s12, s40, 0x36600000
	s_waitcnt lgkmcnt(0)
	v_readfirstlane_b32 s35, v2
	v_mov_b32 v2, v0
	ds_read_b32 v1, v1
	s_addc_u32 s4, s41, 0
	s_and_b32 s13, s4, 0xffff
	s_mov_b32 s15, 0x20000
	s_brev_b32 s14, -2
	s_waitcnt lgkmcnt(0)
	v_lshlrev_b32_e32 v1, 3, v1
	v_cmp_ge_i32_e32 vcc, s2, v1
	v_readfirstlane_b32 s6, v2
	s_cbranch_vccnz .LBB0_1882
	v_ashrrev_i32_e32 v1, 31, v2
	v_lshrrev_b32_e32 v1, 26, v1
	v_add_u32_e32 v1, v2, v1
	s_waitcnt vmcnt(5)
	v_ashrrev_i32_e32 v12, 6, v1
	v_bfe_i32 v1, v2, 27, 1
	s_waitcnt vmcnt(0)
	v_lshlrev_b32_e32 v3, 4, v2
	v_lshrrev_b32_e32 v1, 22, v1
	v_add_u32_e32 v1, v3, v1
	v_and_b32_e32 v1, 0xfffffc00, v1
	v_sub_u32_e32 v1, v3, v1
	v_lshrrev_b32_e32 v4, 4, v1
	v_bitop3_b32 v13, v4, v1, 32 bitop3:0x6c
	v_ashrrev_i32_e32 v1, 31, v1
	v_lshrrev_b32_e32 v1, 26, v1
	v_lshlrev_b32_e32 v4, 3, v12
	v_add_u32_e32 v1, v13, v1
	v_and_b32_e32 v4, -16, v4
	v_ashrrev_i32_e32 v14, 6, v1
	v_add_u32_e32 v3, 0x2000, v3
	v_add_u32_e32 v1, v14, v4
	v_ashrrev_i32_e32 v4, 31, v3
	v_lshrrev_b32_e32 v4, 22, v4
	v_add_u32_e32 v4, v3, v4
	v_ashrrev_i32_e32 v15, 10, v4
	v_mul_i32_i24_e32 v4, 0x400, v15
	v_sub_u32_e32 v3, v3, v4
	s_add_u32 s16, s40, 0x9c00000
	v_lshrrev_b32_e32 v4, 4, v3
	s_addc_u32 s4, s41, 0
	v_bitop3_b32 v3, v4, v3, 32 bitop3:0x6c
	v_lshlrev_b32_e32 v4, 3, v15
	s_add_u32 s20, s40, 0x4dd00000
	v_and_b32_e32 v16, -16, v4
	v_ashrrev_i32_e32 v4, 31, v3
	s_addc_u32 s5, s41, 0
	v_lshrrev_b32_e32 v4, 26, v4
	s_add_i32 s7, 0, 0x20044
	v_add_u32_e32 v17, v3, v4
	v_mov_b32_e32 v4, s7
	ds_read2_b32 v[4:5], v4 offset1:1
	s_add_i32 s7, 0, 0x2004c
	v_mov_b32_e32 v6, s7
	s_add_i32 s7, 0, 0x20054
	v_mov_b32_e32 v8, s7
	s_add_i32 s7, 0, 0x2005c
	v_mov_b32_e32 v10, s7
	s_ashr_i32 s46, s2, 3
	ds_read2_b32 v[6:7], v6 offset1:1
	ds_read2_b32 v[8:9], v8 offset1:1
	ds_read2_b32 v[10:11], v10 offset1:1
	s_waitcnt lgkmcnt(3)
	v_cmp_ge_i32_e32 vcc, s46, v4
	s_add_i32 s7, 0, 0x20064
	v_add_u32_e32 v197, 0x80, v1
	v_cndmask_b32_e64 v4, 0, 1, vcc
	v_cmp_lt_i32_e32 vcc, s46, v5
	s_mov_b32 s8, 0x1fffe0
	s_and_b32 s17, s4, 0xffff
	v_cndmask_b32_e32 v4, 2, v4, vcc
	s_waitcnt lgkmcnt(2)
	v_cmp_lt_i32_e32 vcc, s46, v6
	s_and_b32 s38, s2, 7
	s_and_b32 s21, s5, 0xffff
	v_cndmask_b32_e32 v4, 3, v4, vcc
	v_cmp_lt_i32_e32 vcc, s46, v7
	s_lshl_b32 s5, s38, 19
	s_mov_b32 s22, s14
	v_cndmask_b32_e32 v4, 4, v4, vcc
	s_waitcnt lgkmcnt(1)
	v_cmp_lt_i32_e32 vcc, s46, v8
	s_mov_b32 s23, s15
	s_mov_b32 s18, s14
	v_cndmask_b32_e32 v4, 5, v4, vcc
	v_cmp_lt_i32_e32 vcc, s46, v9
	s_mov_b32 s19, s15
	s_nop 0
	v_cndmask_b32_e32 v4, 6, v4, vcc
	s_waitcnt lgkmcnt(0)
	v_cmp_lt_i32_e32 vcc, s46, v10
	s_nop 1
	v_cndmask_b32_e32 v4, 7, v4, vcc
	v_cmp_lt_i32_e32 vcc, s46, v11
	s_nop 1
	v_cndmask_b32_e32 v10, 8, v4, vcc
	v_mov_b32_e32 v4, s7
	ds_read2_b32 v[4:5], v4 offset1:1
	s_add_i32 s7, 0, 0x2006c
	v_mov_b32_e32 v6, s7
	s_add_i32 s7, 0, 0x20074
	v_mov_b32_e32 v8, s7
	s_add_i32 s7, 0, 0x2007c
	v_mov_b32_e32 v11, s7
	ds_read2_b32 v[6:7], v6 offset1:1
	ds_read2_b32 v[8:9], v8 offset1:1
	ds_read_b32 v11, v11
	s_waitcnt lgkmcnt(3)
	v_cmp_lt_i32_e32 vcc, s46, v4
	s_movk_i32 s7, 0x4200
	s_nop 0
	v_cndmask_b32_e32 v4, 9, v10, vcc
	v_cmp_lt_i32_e32 vcc, s46, v5
	v_ashrrev_i32_e32 v10, 6, v17
	v_add_u32_e32 v196, v10, v16
	v_cndmask_b32_e32 v4, 10, v4, vcc
	s_waitcnt lgkmcnt(2)
	v_cmp_lt_i32_e32 vcc, s46, v6
	v_add_u32_e32 v198, 0x80, v196
	s_nop 0
	v_cndmask_b32_e32 v4, 11, v4, vcc
	v_cmp_lt_i32_e32 vcc, s46, v7
	s_nop 1
	v_cndmask_b32_e32 v4, 12, v4, vcc
	s_waitcnt lgkmcnt(1)
	v_cmp_lt_i32_e32 vcc, s46, v8
	s_nop 1
	v_cndmask_b32_e32 v4, 13, v4, vcc
	v_cmp_lt_i32_e32 vcc, s46, v9
	s_nop 1
	v_cndmask_b32_e32 v4, 14, v4, vcc
	s_waitcnt lgkmcnt(0)
	v_cmp_lt_i32_e32 vcc, s46, v11
	s_nop 1
	v_cndmask_b32_e32 v194, 15, v4, vcc
	v_lshlrev_b32_e32 v4, 2, v194
	v_add_u32_e32 v4, 0, v4
	v_add_u32_e32 v4, 0x20000, v4
	ds_read2_b32 v[4:5], v4 offset1:16
	v_mul_lo_u32 v11, v194, s7
	s_ashr_i32 s7, s6, 8
	s_waitcnt lgkmcnt(0)
	v_sub_u32_e32 v5, s46, v5
	v_lshlrev_b32_e32 v16, 8, v5
	v_add_u32_e32 v5, v16, v1
	v_add_u32_e32 v18, -1, v4
	v_min_i32_e32 v4, v5, v18
	v_add_u32_e32 v6, v16, v197
	v_add_u32_e32 v8, v16, v196
	v_add_u32_e32 v4, v4, v11
	v_min_i32_e32 v6, v6, v18
	v_min_i32_e32 v8, v8, v18
	v_ashrrev_i32_e32 v5, 31, v4
	v_add_u32_e32 v6, v6, v11
	v_add_u32_e32 v8, v8, v11
	v_lshl_add_u64 v[4:5], v[4:5], 2, s[26:27]
	v_ashrrev_i32_e32 v7, 31, v6
	v_ashrrev_i32_e32 v9, 31, v8
	v_lshl_add_u64 v[6:7], v[6:7], 2, s[26:27]
	v_lshl_add_u64 v[8:9], v[8:9], 2, s[26:27]
	global_load_dword v19, v[4:5], off
	global_load_dword v20, v[6:7], off
	global_load_dword v21, v[8:9], off
	v_add_u32_e32 v4, v16, v198
	v_min_i32_e32 v4, v4, v18
	v_add_u32_e32 v4, v4, v11
	v_ashrrev_i32_e32 v5, 31, v4
	v_lshl_add_u64 v[4:5], v[4:5], 2, s[26:27]
	global_load_dword v4, v[4:5], off
	v_mul_i32_i24_e32 v6, 64, v14
	v_sub_u32_e32 v6, v13, v6
	v_mov_b32_e32 v7, 1
	v_lshlrev_b32_e32 v5, 5, v12
	v_ashrrev_i16_sdwa v6, v7, sext(v6) dst_sel:DWORD dst_unused:UNUSED_PAD src0_sel:DWORD src1_sel:BYTE_0
	v_and_b32_e32 v5, 32, v5
	v_bfe_i32 v6, v6, 0, 16
	v_add_lshl_u32 v199, v5, v6, 1
	v_and_b32_e32 v6, 0xc0, v17
	v_sub_u32_e32 v3, v3, v6
	v_lshlrev_b32_e32 v5, 5, v15
	v_ashrrev_i16_sdwa v3, v7, sext(v3) dst_sel:DWORD dst_unused:UNUSED_PAD src0_sel:DWORD src1_sel:BYTE_0
	v_and_b32_e32 v5, 32, v5
	v_bfe_i32 v3, v3, 0, 16
	v_add_lshl_u32 v201, v5, v3, 1
	v_lshlrev_b32_e32 v8, 1, v1
	v_lshrrev_b32_e32 v9, 2, v1
	v_and_b32_e32 v11, 3, v14
	v_and_b32_e32 v8, 24, v8
	v_and_b32_e32 v9, 4, v9
	v_and_or_b32 v11, v1, s8, v11
	v_or3_b32 v8, v11, v9, v8
	v_lshl_add_u32 v200, v8, 11, v199
	v_and_b32_e32 v8, 3, v10
	v_lshlrev_b32_e32 v6, 1, v196
	v_lshrrev_b32_e32 v7, 2, v196
	v_and_or_b32 v8, v196, s8, v8
	s_ashr_i32 s8, s6, 6
	v_and_b32_e32 v6, 24, v6
	v_and_b32_e32 v7, 4, v7
	s_lshl_b32 s4, s8, 10
	v_or3_b32 v6, v8, v7, v6
	s_add_i32 s47, s4, 0
	v_lshl_add_u32 v202, v6, 11, v201
	s_add_i32 s48, s47, 0x10000
	s_mov_b32 m0, s48
	s_waitcnt vmcnt(3)
	v_lshlrev_b32_e32 v3, 10, v19
	v_and_b32_e32 v3, 0xfffff800, v3
	v_add_u32_e32 v195, v3, v199
	s_waitcnt vmcnt(2)
	v_lshlrev_b32_e32 v3, 10, v20
	v_and_b32_e32 v3, 0xfffff800, v3
	v_add_u32_e32 v218, v3, v199
	s_waitcnt vmcnt(1)
	v_lshlrev_b32_e32 v3, 10, v21
	v_and_b32_e32 v3, 0xfffff800, v3
	v_add_u32_e32 v217, v3, v201
	s_waitcnt vmcnt(0)
	v_lshlrev_b32_e32 v3, 10, v4
	v_and_b32_e32 v3, 0xfffff800, v3
	v_add_u32_e32 v219, v3, v201
	v_lshlrev_b32_e32 v3, 22, v194
	v_or_b32_e32 v220, s5, v3
	s_mov_b64 s[4:5], exec
	v_readfirstlane_b32 s9, v220
	s_nop 4
	buffer_load_dwordx4 v200, s[16:19], s9 offen lds
	s_mov_b64 exec, s[4:5]
	s_add_i32 s49, s47, 0x12000
	s_mov_b64 s[4:5], exec
	s_mov_b32 m0, s49
	s_nop 0
	buffer_load_dwordx4 v202, s[16:19], s9 offen lds
	s_mov_b64 exec, s[4:5]
	s_add_i32 s50, s47, 0x14000
	v_or_b32_e32 v3, 0x40000, v220
	s_mov_b64 s[4:5], exec
	s_mov_b32 m0, s50
	v_readfirstlane_b32 s9, v3
	s_nop 4
	buffer_load_dwordx4 v200, s[16:19], s9 offen lds
	s_mov_b64 exec, s[4:5]
	s_add_i32 s51, s47, 0x16000
	s_mov_b64 s[4:5], exec
	s_mov_b32 m0, s51
	s_nop 0
	buffer_load_dwordx4 v202, s[16:19], s9 offen lds
	s_mov_b64 exec, s[4:5]
	s_mov_b32 m0, s47
	s_add_i32 s52, s47, 0x2000
	buffer_load_dwordx4 v195, s[20:23], 0 offen lds
	s_mov_b32 m0, s52
	s_add_i32 s53, s47, 0x4000
	buffer_load_dwordx4 v217, s[20:23], 0 offen lds
	s_mov_b32 m0, s53
	s_add_i32 s56, s47, 0x6000
	buffer_load_dwordx4 v218, s[20:23], 0 offen lds
	s_mov_b32 m0, s56
	s_cmp_eq_u32 s7, 1
	buffer_load_dwordx4 v219, s[20:23], 0 offen lds
	s_cselect_b64 s[10:11], -1, 0
	s_cmp_lg_u32 s7, 1
	s_cbranch_scc1 .LBB0_1834
	s_barrier
.LBB0_1834:
	v_and_b32_e32 v203, 15, v2
	s_add_u32 s28, s40, 0xc000
	v_bfe_u32 v204, v2, 4, 2
	v_lshlrev_b32_e32 v3, 6, v203
	v_lshlrev_b32_e32 v2, 2, v2
	s_addc_u32 s29, s41, 0
	v_lshl_or_b32 v3, v204, 4, v3
	s_lshl_b32 s4, s7, 13
	v_and_b32_e32 v4, 32, v2
	v_bitop3_b32 v2, v3, s4, v4 bitop3:0xde
	s_lshl_b32 s4, s8, 5
	s_and_b32 s8, s4, 0x60
	s_waitcnt vmcnt(2)
	s_lshl_b32 s4, s8, 7
	v_bitop3_b32 v3, v3, s4, v4 bitop3:0xde
	s_add_i32 s57, s47, 0x18000
	s_movk_i32 s9, 0x80
	v_or_b32_e32 v4, 0x80, v220
	s_mov_b32 s18, s14
	s_mov_b32 s19, s15
	s_mov_b64 s[4:5], exec
	s_barrier
	s_mov_b32 m0, s57
	v_readfirstlane_b32 s22, v4
	s_nop 4
	buffer_load_dwordx4 v200, s[16:19], s22 offen lds
	s_mov_b64 exec, s[4:5]
	s_add_i32 s58, s47, 0x1a000
	s_mov_b64 s[4:5], exec
	s_mov_b32 m0, s58
	s_nop 0
	buffer_load_dwordx4 v202, s[16:19], s22 offen lds
	s_mov_b64 exec, s[4:5]
	s_add_i32 s59, s47, 0x8000
	s_mov_b32 s22, s14
	s_mov_b32 s23, s15
	s_mov_b32 m0, s59
	s_add_i32 s60, s47, 0xa000
	buffer_load_dwordx4 v195, s[20:23], s9 offen lds
	s_mov_b32 m0, s60
	s_add_i32 s61, s47, 0x1c000
	buffer_load_dwordx4 v217, s[20:23], s9 offen lds
	v_or_b32_e32 v4, 0x40080, v220
	s_mov_b64 s[4:5], exec
	s_mov_b32 m0, s61
	v_readfirstlane_b32 s9, v4
	s_nop 4
	buffer_load_dwordx4 v200, s[16:19], s9 offen lds
	s_mov_b64 exec, s[4:5]
	s_add_i32 s62, s47, 0x1e000
	s_mov_b64 s[4:5], exec
	s_mov_b32 m0, s62
	s_nop 0
	buffer_load_dwordx4 v202, s[16:19], s9 offen lds
	s_mov_b64 exec, s[4:5]
	s_add_i32 s63, s47, 0xc000
	s_cmpk_lt_u32 s6, 0x100
	s_waitcnt vmcnt(6)
	s_cselect_b64 s[30:31], -1, 0
	s_lshl_b32 s6, s7, 16
	v_and_b32_e32 v4, 63, v0
	s_or_b32 s66, s8, s6
	s_add_i32 s6, 0, 0x20080
	v_add_u32_e32 v206, 0, v3
	s_mov_b32 s64, 0
	v_cmp_eq_u32_e64 s[4:5], 0, v4
	s_add_i32 s65, s47, 0xe000
	v_mov_b32_e32 v205, s6
	s_add_i32 s67, 0, 0x20044
	s_add_i32 s68, 0, 0x2004c
	s_add_i32 s69, 0, 0x20054
	s_add_i32 s70, 0, 0x2005c
	s_add_i32 s71, 0, 0x20064
	s_add_i32 s72, 0, 0x2006c
	s_add_i32 s73, 0, 0x20074
	s_add_i32 s74, 0, 0x2007c
	s_movk_i32 s75, 0x4200
	v_add_u32_e32 v207, 0x10000, v206
	v_add_u32_e32 v208, 0x14000, v206
	v_add_u32_e32 v209, 0, v2
	s_mov_b32 s22, s14
	s_mov_b32 s23, s15
	s_mov_b32 s18, s14
	s_mov_b32 s19, s15
	v_mov_b32_e32 v210, 0
	s_brev_b32 s34, 60
	s_barrier
	s_branch .LBB0_1845

.LBB0_1856:
	s_add_i32 s81, s78, 0xffffff80
	s_cmp_eq_u32 s39, 12
	v_add_u32_e32 v2, s78, v220
	s_cselect_b64 vcc, -1, 0
	v_cndmask_b32_e32 v222, v2, v221, vcc
	ds_read_b128 v[2:5], v207
	ds_read_b128 v[6:9], v207 offset:1024
	ds_read_b128 v[10:13], v207 offset:2048
	ds_read_b128 v[14:17], v207 offset:3072
	ds_read_b128 v[18:21], v208
	ds_read_b128 v[22:25], v208 offset:1024
	ds_read_b128 v[26:29], v208 offset:2048
	ds_read_b128 v[30:33], v208 offset:3072
	s_and_b64 s[8:9], vcc, exec
	s_cselect_b32 s80, 0, s78
	s_or_b32 s79, s80, 0x80
	v_add_u32_e32 v225, 0x80, v222
	v_cndmask_b32_e32 v223, v195, v212, vcc
	v_cndmask_b32_e32 v226, v218, v213, vcc
	v_cndmask_b32_e32 v224, v217, v214, vcc
	v_cndmask_b32_e32 v227, v219, v215, vcc
	s_mov_b32 m0, s63
	ds_read_b128 v[34:37], v209
	ds_read_b128 v[38:41], v209 offset:1024
	ds_read_b128 v[42:45], v209 offset:2048
	ds_read_b128 v[46:49], v209 offset:3072
	ds_read_b128 v[50:53], v209 offset:4096
	ds_read_b128 v[54:57], v209 offset:5120
	ds_read_b128 v[58:61], v209 offset:6144
	ds_read_b128 v[62:65], v209 offset:7168
	buffer_load_dwordx4 v218, s[20:23], s81 offen lds
	s_mov_b32 m0, s65
	s_nop 0
	buffer_load_dwordx4 v219, s[20:23], s81 offen lds
	s_waitcnt vmcnt(8)
	s_waitcnt lgkmcnt(0)
	s_barrier
	s_setprio 1
	s_waitcnt lgkmcnt(6)
	v_mfma_f32_16x16x128_f8f6f4 v[182:185], v[2:9], v[34:41], v[182:185]
	v_mfma_f32_16x16x128_f8f6f4 v[178:181], v[10:17], v[34:41], v[178:181]
	s_waitcnt lgkmcnt(4)
	v_mfma_f32_16x16x128_f8f6f4 v[170:173], v[2:9], v[42:49], v[170:173]
	v_mfma_f32_16x16x128_f8f6f4 v[166:169], v[10:17], v[42:49], v[166:169]
	s_waitcnt lgkmcnt(2)
	v_mfma_f32_16x16x128_f8f6f4 v[154:157], v[2:9], v[50:57], v[154:157]
	v_mfma_f32_16x16x128_f8f6f4 v[150:153], v[10:17], v[50:57], v[150:153]
	s_waitcnt lgkmcnt(0)
	v_mfma_f32_16x16x128_f8f6f4 v[138:141], v[2:9], v[58:65], v[138:141]
	v_mfma_f32_16x16x128_f8f6f4 v[134:137], v[10:17], v[58:65], v[134:137]
	s_setprio 0
	s_setprio 1
	v_mfma_f32_16x16x128_f8f6f4 v[190:193], v[18:25], v[34:41], v[190:193]
	v_mfma_f32_16x16x128_f8f6f4 v[186:189], v[26:33], v[34:41], v[186:189]
	v_mfma_f32_16x16x128_f8f6f4 v[174:177], v[18:25], v[42:49], v[174:177]
	v_mfma_f32_16x16x128_f8f6f4 v[162:165], v[26:33], v[42:49], v[162:165]
	v_mfma_f32_16x16x128_f8f6f4 v[158:161], v[18:25], v[50:57], v[158:161]
	v_mfma_f32_16x16x128_f8f6f4 v[146:149], v[26:33], v[50:57], v[146:149]
	v_mfma_f32_16x16x128_f8f6f4 v[142:145], v[18:25], v[58:65], v[142:145]
	v_mfma_f32_16x16x128_f8f6f4 v[130:133], v[26:33], v[58:65], v[130:133]
	s_setprio 0
	s_barrier
	ds_read_b128 v[34:37], v209 offset:16384
	ds_read_b128 v[38:41], v209 offset:17408
	ds_read_b128 v[42:45], v209 offset:18432
	ds_read_b128 v[46:49], v209 offset:19456
	ds_read_b128 v[50:53], v209 offset:20480
	ds_read_b128 v[54:57], v209 offset:21504
	ds_read_b128 v[58:61], v209 offset:22528
	ds_read_b128 v[62:65], v209 offset:23552
	s_mov_b64 s[8:9], exec
	s_mov_b32 m0, s48
	v_readfirstlane_b32 s81, v222
	s_nop 4
	buffer_load_dwordx4 v200, s[16:19], s81 offen lds
	s_mov_b64 exec, s[8:9]
	s_mov_b64 s[8:9], exec
	s_mov_b32 m0, s49
	s_nop 0
	buffer_load_dwordx4 v202, s[16:19], s81 offen lds
	s_mov_b64 exec, s[8:9]
	v_add_u32_e32 v228, 0x40000, v222
	s_mov_b64 s[8:9], exec
	s_mov_b32 m0, s50
	v_readfirstlane_b32 s81, v228
	s_nop 4
	buffer_load_dwordx4 v200, s[16:19], s81 offen lds
	s_mov_b64 exec, s[8:9]
	s_mov_b64 s[8:9], exec
	s_mov_b32 m0, s51
	s_nop 0
	buffer_load_dwordx4 v202, s[16:19], s81 offen lds
	s_mov_b64 exec, s[8:9]
	s_mov_b32 m0, s47
	s_nop 0
	buffer_load_dwordx4 v223, s[20:23], s80 offen lds
	s_mov_b32 m0, s52
	s_nop 0
	buffer_load_dwordx4 v224, s[20:23], s80 offen lds
	s_waitcnt vmcnt(8)
	s_waitcnt lgkmcnt(0)
	s_barrier
	s_setprio 1
	s_waitcnt lgkmcnt(6)
	v_mfma_f32_16x16x128_f8f6f4 v[118:121], v[2:9], v[34:41], v[118:121]
	v_mfma_f32_16x16x128_f8f6f4 v[114:117], v[10:17], v[34:41], v[114:117]
	s_waitcnt lgkmcnt(4)
	v_mfma_f32_16x16x128_f8f6f4 v[102:105], v[2:9], v[42:49], v[102:105]
	v_mfma_f32_16x16x128_f8f6f4 v[98:101], v[10:17], v[42:49], v[98:101]
	s_waitcnt lgkmcnt(2)
	v_mfma_f32_16x16x128_f8f6f4 v[86:89], v[2:9], v[50:57], v[86:89]
	v_mfma_f32_16x16x128_f8f6f4 v[82:85], v[10:17], v[50:57], v[82:85]
	s_waitcnt lgkmcnt(0)
	v_mfma_f32_16x16x128_f8f6f4 v[70:73], v[2:9], v[58:65], v[70:73]
	v_mfma_f32_16x16x128_f8f6f4 v[66:69], v[10:17], v[58:65], v[66:69]
	s_setprio 0
	s_setprio 1
	v_mfma_f32_16x16x128_f8f6f4 v[126:129], v[18:25], v[34:41], v[126:129]
	v_mfma_f32_16x16x128_f8f6f4 v[122:125], v[26:33], v[34:41], v[122:125]
	v_mfma_f32_16x16x128_f8f6f4 v[110:113], v[18:25], v[42:49], v[110:113]
	v_mfma_f32_16x16x128_f8f6f4 v[106:109], v[26:33], v[42:49], v[106:109]
	v_mfma_f32_16x16x128_f8f6f4 v[94:97], v[18:25], v[50:57], v[94:97]
	v_mfma_f32_16x16x128_f8f6f4 v[90:93], v[26:33], v[50:57], v[90:93]
	v_mfma_f32_16x16x128_f8f6f4 v[78:81], v[18:25], v[58:65], v[78:81]
	v_mfma_f32_16x16x128_f8f6f4 v[74:77], v[26:33], v[58:65], v[74:77]
	s_setprio 0
	s_barrier
	v_add_u32_e32 v14, 0x18000, v206
	v_add_u32_e32 v30, 0x1c000, v206
	ds_read_b128 v[2:5], v14
	ds_read_b128 v[6:9], v14 offset:1024
	ds_read_b128 v[10:13], v14 offset:2048
	ds_read_b128 v[14:17], v14 offset:3072
	ds_read_b128 v[18:21], v30
	ds_read_b128 v[22:25], v30 offset:1024
	ds_read_b128 v[26:29], v30 offset:2048
	ds_read_b128 v[30:33], v30 offset:3072
	s_mov_b32 m0, s53
	ds_read_b128 v[34:37], v209 offset:32768
	ds_read_b128 v[38:41], v209 offset:33792
	ds_read_b128 v[42:45], v209 offset:34816
	ds_read_b128 v[46:49], v209 offset:35840
	ds_read_b128 v[50:53], v209 offset:36864
	ds_read_b128 v[54:57], v209 offset:37888
	ds_read_b128 v[58:61], v209 offset:38912
	ds_read_b128 v[62:65], v209 offset:39936
	buffer_load_dwordx4 v226, s[20:23], s80 offen lds
	s_mov_b32 m0, s56
	s_nop 0
	buffer_load_dwordx4 v227, s[20:23], s80 offen lds
	s_waitcnt vmcnt(8)
	s_waitcnt lgkmcnt(0)
	s_barrier
	s_setprio 1
	s_waitcnt lgkmcnt(6)
	v_mfma_f32_16x16x128_f8f6f4 v[182:185], v[2:9], v[34:41], v[182:185]
	v_mfma_f32_16x16x128_f8f6f4 v[178:181], v[10:17], v[34:41], v[178:181]
	s_waitcnt lgkmcnt(4)
	v_mfma_f32_16x16x128_f8f6f4 v[170:173], v[2:9], v[42:49], v[170:173]
	v_mfma_f32_16x16x128_f8f6f4 v[166:169], v[10:17], v[42:49], v[166:169]
	s_waitcnt lgkmcnt(2)
	v_mfma_f32_16x16x128_f8f6f4 v[154:157], v[2:9], v[50:57], v[154:157]
	v_mfma_f32_16x16x128_f8f6f4 v[150:153], v[10:17], v[50:57], v[150:153]
	s_waitcnt lgkmcnt(0)
	v_mfma_f32_16x16x128_f8f6f4 v[138:141], v[2:9], v[58:65], v[138:141]
	v_mfma_f32_16x16x128_f8f6f4 v[134:137], v[10:17], v[58:65], v[134:137]
	s_setprio 0
	s_setprio 1
	v_mfma_f32_16x16x128_f8f6f4 v[190:193], v[18:25], v[34:41], v[190:193]
	v_mfma_f32_16x16x128_f8f6f4 v[186:189], v[26:33], v[34:41], v[186:189]
	v_mfma_f32_16x16x128_f8f6f4 v[174:177], v[18:25], v[42:49], v[174:177]
	v_mfma_f32_16x16x128_f8f6f4 v[162:165], v[26:33], v[42:49], v[162:165]
	v_mfma_f32_16x16x128_f8f6f4 v[158:161], v[18:25], v[50:57], v[158:161]
	v_mfma_f32_16x16x128_f8f6f4 v[146:149], v[26:33], v[50:57], v[146:149]
	v_mfma_f32_16x16x128_f8f6f4 v[142:145], v[18:25], v[58:65], v[142:145]
	v_mfma_f32_16x16x128_f8f6f4 v[130:133], v[26:33], v[58:65], v[130:133]
	s_setprio 0
	s_barrier
	ds_read_b128 v[34:37], v209 offset:49152
	ds_read_b128 v[38:41], v209 offset:50176
	ds_read_b128 v[42:45], v209 offset:51200
	ds_read_b128 v[46:49], v209 offset:52224
	ds_read_b128 v[50:53], v209 offset:53248
	ds_read_b128 v[54:57], v209 offset:54272
	ds_read_b128 v[58:61], v209 offset:55296
	ds_read_b128 v[62:65], v209 offset:56320
	s_mov_b64 s[8:9], exec
	s_mov_b32 m0, s57
	v_readfirstlane_b32 s80, v225
	s_nop 4
	buffer_load_dwordx4 v200, s[16:19], s80 offen lds
	s_mov_b64 exec, s[8:9]
	s_mov_b64 s[8:9], exec
	s_mov_b32 m0, s58
	s_nop 0
	buffer_load_dwordx4 v202, s[16:19], s80 offen lds
	s_mov_b64 exec, s[8:9]
	v_add_u32_e32 v222, 0x40080, v222
	s_mov_b64 s[8:9], exec
	s_mov_b32 m0, s61
	v_readfirstlane_b32 s80, v222
	s_nop 4
	buffer_load_dwordx4 v200, s[16:19], s80 offen lds
	s_mov_b64 exec, s[8:9]
	s_mov_b64 s[8:9], exec
	s_mov_b32 m0, s62
	s_nop 0
	buffer_load_dwordx4 v202, s[16:19], s80 offen lds
	s_mov_b64 exec, s[8:9]
	s_mov_b32 m0, s59
	s_nop 0
	buffer_load_dwordx4 v223, s[20:23], s79 offen lds
	s_mov_b32 m0, s60
	s_nop 0
	buffer_load_dwordx4 v224, s[20:23], s79 offen lds
	s_waitcnt vmcnt(8)
	s_waitcnt lgkmcnt(0)
	s_barrier
	s_setprio 1
	s_waitcnt lgkmcnt(6)
	v_mfma_f32_16x16x128_f8f6f4 v[118:121], v[2:9], v[34:41], v[118:121]
	v_mfma_f32_16x16x128_f8f6f4 v[114:117], v[10:17], v[34:41], v[114:117]
	s_waitcnt lgkmcnt(4)
	v_mfma_f32_16x16x128_f8f6f4 v[102:105], v[2:9], v[42:49], v[102:105]
	v_mfma_f32_16x16x128_f8f6f4 v[98:101], v[10:17], v[42:49], v[98:101]
	s_waitcnt lgkmcnt(2)
	v_mfma_f32_16x16x128_f8f6f4 v[86:89], v[2:9], v[50:57], v[86:89]
	v_mfma_f32_16x16x128_f8f6f4 v[82:85], v[10:17], v[50:57], v[82:85]
	s_waitcnt lgkmcnt(0)
	v_mfma_f32_16x16x128_f8f6f4 v[70:73], v[2:9], v[58:65], v[70:73]
	v_mfma_f32_16x16x128_f8f6f4 v[66:69], v[10:17], v[58:65], v[66:69]
	s_setprio 0
	s_setprio 1
	v_mfma_f32_16x16x128_f8f6f4 v[126:129], v[18:25], v[34:41], v[126:129]
	v_mfma_f32_16x16x128_f8f6f4 v[122:125], v[26:33], v[34:41], v[122:125]
	v_mfma_f32_16x16x128_f8f6f4 v[110:113], v[18:25], v[42:49], v[110:113]
	v_mfma_f32_16x16x128_f8f6f4 v[106:109], v[26:33], v[42:49], v[106:109]
	v_mfma_f32_16x16x128_f8f6f4 v[94:97], v[18:25], v[50:57], v[94:97]
	v_mfma_f32_16x16x128_f8f6f4 v[90:93], v[26:33], v[50:57], v[90:93]
	v_mfma_f32_16x16x128_f8f6f4 v[78:81], v[18:25], v[58:65], v[78:81]
	v_mfma_f32_16x16x128_f8f6f4 v[74:77], v[26:33], v[58:65], v[74:77]
	s_setprio 0
	s_barrier
	s_add_i32 s39, s39, 2
	s_addk_i32 s78, 0x100
	s_cmp_gt_u32 s39, 13
	s_cbranch_scc0 .LBB0_1856
	s_and_b64 vcc, exec, s[30:31]
	s_cbranch_vccz .LBB0_1875
	s_barrier

.LBB0_1902:
	s_or_b64 exec, exec, s[6:7]
	v_bfe_i32 v5, v2, 27, 1
	s_waitcnt vmcnt(0)
	v_lshlrev_b32_e32 v3, 4, v2
	v_lshrrev_b32_e32 v5, 22, v5
	v_add_u32_e32 v5, v3, v5
	v_and_b32_e32 v5, 0xfffffc00, v5
	v_sub_u32_e32 v5, v3, v5
	v_lshrrev_b32_e32 v6, 4, v5
	v_bitop3_b32 v6, v6, v5, 32 bitop3:0x6c
	v_ashrrev_i32_e32 v5, 31, v5
	v_lshrrev_b32_e32 v5, 26, v5
	v_ashrrev_i32_e32 v4, 31, v2
	v_add_u32_e32 v5, v6, v5
	v_lshrrev_b32_e32 v4, 26, v4
	v_ashrrev_i32_e32 v5, 6, v5
	v_add_u32_e32 v4, v2, v4
	v_mul_i32_i24_e32 v8, 64, v5
	v_ashrrev_i32_e32 v4, 6, v4
	v_sub_u32_e32 v6, v6, v8
	v_mov_b32_e32 v8, 1
	v_lshlrev_b32_e32 v7, 3, v4
	v_lshlrev_b32_e32 v4, 5, v4
	v_ashrrev_i16_sdwa v6, v8, sext(v6) dst_sel:DWORD dst_unused:UNUSED_PAD src0_sel:DWORD src1_sel:BYTE_0
	v_and_b32_e32 v4, 32, v4
	v_bfe_i32 v6, v6, 0, 16
	v_add_u32_e32 v3, 0x2000, v3
	v_add_lshl_u32 v4, v4, v6, 1
	v_ashrrev_i32_e32 v6, 31, v3
	v_lshrrev_b32_e32 v6, 22, v6
	v_add_u32_e32 v6, v3, v6
	v_ashrrev_i32_e32 v6, 10, v6
	v_mul_i32_i24_e32 v9, 0x400, v6
	v_sub_u32_e32 v3, v3, v9
	v_lshrrev_b32_e32 v9, 4, v3
	v_bitop3_b32 v3, v9, v3, 32 bitop3:0x6c
	v_ashrrev_i32_e32 v10, 31, v3
	v_lshrrev_b32_e32 v10, 26, v10
	v_add_u32_e32 v10, v3, v10
	v_ashrrev_i32_e32 v11, 6, v10
	v_and_b32_e32 v10, 0xc0, v10
	v_sub_u32_e32 v3, v3, v10
	v_lshlrev_b32_e32 v9, 3, v6
	v_lshlrev_b32_e32 v6, 5, v6
	v_ashrrev_i16_sdwa v3, v8, sext(v3) dst_sel:DWORD dst_unused:UNUSED_PAD src0_sel:DWORD src1_sel:BYTE_0
	v_and_b32_e32 v7, -16, v7
	v_and_b32_e32 v6, 32, v6
	v_bfe_i32 v3, v3, 0, 16
	v_add_u32_e32 v7, v5, v7
	v_add_lshl_u32 v3, v6, v3, 1
	v_lshlrev_b32_e32 v6, 21, v208
	s_lshl_b32 s6, s58, 18
	v_add_u32_e32 v209, s6, v6
	v_lshlrev_b32_e32 v6, 1, v7
	v_lshrrev_b32_e32 v8, 2, v7
	v_and_b32_e32 v5, 3, v5
	s_mov_b32 s7, 0x3fffe0
	v_and_b32_e32 v9, -16, v9
	s_lshl_b32 s92, s34, 18
	v_and_b32_e32 v6, 24, v6
	v_and_b32_e32 v8, 4, v8
	v_and_or_b32 v5, v7, s7, v5
	v_add_u32_e32 v9, v11, v9
	s_add_u32 s16, s40, 0x19c00000
	v_or3_b32 v5, v5, v8, v6
	v_lshl_add_u32 v194, v7, 10, v4
	s_addc_u32 s6, s41, 0
	v_lshl_add_u32 v196, v5, 10, v4
	v_lshlrev_b32_e32 v4, 1, v9
	v_lshrrev_b32_e32 v5, 2, v9
	v_and_b32_e32 v6, 3, v11
	s_ashr_i32 s9, s31, 6
	v_and_b32_e32 v4, 24, v4
	v_and_b32_e32 v5, 4, v5
	v_and_or_b32 v6, v9, s7, v6
	s_and_b32 s17, s6, 0xffff
	s_lshl_b32 s6, s9, 10
	s_barrier
	v_or3_b32 v4, v6, v5, v4
	s_add_i32 s59, s6, 0
	v_lshl_add_u32 v195, v9, 10, v3
	s_ashr_i32 s8, s31, 8
	v_lshl_add_u32 v197, v4, 10, v3
	s_mov_b32 s19, 0x20000
	s_brev_b32 s18, -2
	s_add_i32 s60, s59, 0x10000
	s_mov_b64 s[6:7], exec
	s_mov_b32 m0, s60
	v_readfirstlane_b32 s10, v209
	s_nop 4
	buffer_load_dwordx4 v196, s[16:19], s10 offen lds
	s_mov_b64 exec, s[6:7]
	s_add_i32 s61, s59, 0x12000
	s_mov_b64 s[6:7], exec
	s_mov_b32 m0, s61
	s_nop 0
	buffer_load_dwordx4 v197, s[16:19], s10 offen lds
	s_mov_b64 exec, s[6:7]
	s_add_i32 s62, s59, 0x14000
	v_or_b32_e32 v3, 0x20000, v209
	s_mov_b64 s[6:7], exec
	s_mov_b32 m0, s62
	v_readfirstlane_b32 s10, v3
	s_nop 4
	buffer_load_dwordx4 v196, s[16:19], s10 offen lds
	s_mov_b64 exec, s[6:7]
	s_add_i32 s63, s59, 0x16000
	s_mov_b64 s[6:7], exec
	s_mov_b32 m0, s63
	s_nop 0
	buffer_load_dwordx4 v197, s[16:19], s10 offen lds
	s_mov_b64 exec, s[6:7]
	s_mov_b32 m0, s59
	s_add_i32 s64, s59, 0x2000
	buffer_load_dwordx4 v194, s[12:15], s92 offen lds
	s_mov_b32 m0, s64
	s_add_i32 s65, s59, 0x4000
	buffer_load_dwordx4 v195, s[12:15], s92 offen lds
	s_or_b32 s6, s92, 0x20000
	s_mov_b32 m0, s65
	s_add_i32 s66, s59, 0x6000
	buffer_load_dwordx4 v194, s[12:15], s6 offen lds
	s_mov_b32 m0, s66
	s_cmp_eq_u32 s8, 1
	buffer_load_dwordx4 v195, s[12:15], s6 offen lds
	s_cselect_b64 s[20:21], -1, 0
	s_cmp_lg_u32 s8, 1
	s_cbranch_scc1 .LBB0_1912
	s_barrier
.LBB0_1912:
	s_add_u32 s22, s40, 0x3b000000
	s_addc_u32 s23, s41, 0
	s_add_u32 s28, s40, 0x500000
	s_addc_u32 s29, s41, 0
	s_ashr_i32 s6, s30, 31
	v_bfe_u32 v198, v2, 4, 2
	s_lshr_b32 s6, s6, 25
	v_and_b32_e32 v199, 15, v2
	s_add_i32 s6, s30, s6
	v_lshlrev_b32_e32 v3, 4, v198
	v_lshlrev_b32_e32 v2, 2, v2
	s_ashr_i32 s67, s6, 7
	v_lshl_or_b32 v3, v199, 6, v3
	s_lshl_b32 s6, s8, 13
	v_and_b32_e32 v4, 32, v2
	v_bitop3_b32 v2, v3, s6, v4 bitop3:0xde
	s_lshl_b32 s6, s9, 5
	s_and_b32 s69, s6, 0x60
	s_waitcnt vmcnt(2)
	s_lshl_b32 s6, s69, 7
	s_lshl_b32 s68, s8, 6
	v_bitop3_b32 v3, v3, s6, v4 bitop3:0xde
	s_add_i32 s70, s59, 0x18000
	v_or_b32_e32 v4, 0x80, v209
	s_mov_b64 s[6:7], exec
	s_barrier
	s_mov_b32 m0, s70
	v_readfirstlane_b32 s8, v4
	s_nop 4
	buffer_load_dwordx4 v196, s[16:19], s8 offen lds
	s_mov_b64 exec, s[6:7]
	s_add_i32 s71, s59, 0x1a000
	s_mov_b64 s[6:7], exec
	s_mov_b32 m0, s71
	s_nop 0
	buffer_load_dwordx4 v197, s[16:19], s8 offen lds
	s_mov_b64 exec, s[6:7]
	s_add_i32 s72, s59, 0x8000
	s_or_b32 s6, s92, 0x80
	s_mov_b32 m0, s72
	s_add_i32 s73, s59, 0xa000
	buffer_load_dwordx4 v194, s[12:15], s6 offen lds
	s_mov_b32 m0, s73
	s_add_i32 s74, s59, 0x1c000
	buffer_load_dwordx4 v195, s[12:15], s6 offen lds
	v_or_b32_e32 v4, 0x20080, v209
	s_mov_b64 s[6:7], exec
	s_mov_b32 m0, s74
	v_readfirstlane_b32 s8, v4
	s_nop 4
	buffer_load_dwordx4 v196, s[16:19], s8 offen lds
	s_mov_b64 exec, s[6:7]
	s_add_i32 s75, s59, 0x1e000
	s_mov_b64 s[6:7], exec
	s_mov_b32 m0, s75
	s_nop 0
	buffer_load_dwordx4 v197, s[16:19], s8 offen lds
	s_mov_b64 exec, s[6:7]
	s_cmpk_gt_i32 s30, 0x7f
	s_cselect_b64 s[6:7], -1, 0
	s_add_i32 s76, s67, -2
	s_add_i32 s77, s59, 0xc000
	s_waitcnt vmcnt(6)
	s_cmpk_lt_u32 s31, 0x100
	s_cselect_b64 s[30:31], -1, 0
	s_add_i32 s8, 0, 0x20080
	v_cndmask_b32_e64 v4, 0, 1, s[6:7]
	s_mov_b32 s35, 0
	s_add_i32 s78, s59, 0xe000
	v_mov_b32_e32 v200, s8
	s_add_i32 s79, 0, 0x20044
	s_add_i32 s80, 0, 0x2004c
	s_add_i32 s81, 0, 0x20054
	s_add_i32 s82, 0, 0x2005c
	s_add_i32 s83, 0, 0x20064
	s_add_i32 s84, 0, 0x2006c
	s_add_i32 s85, 0, 0x20074
	s_add_i32 s86, 0, 0x2007c
	v_cmp_ne_u32_e64 s[6:7], 1, v4
	v_mov_b32_e32 v201, 0
	v_mov_b32_e32 v202, 1
	v_add_u32_e32 v203, 0, v3
	v_add_u32_e32 v204, 0, v2
	s_movk_i32 s87, 0x4200
	s_mov_b32 s89, 0
	s_barrier
	s_branch .LBB0_1923

.LBB0_1944:
	v_add_u32_e32 v14, 0x10000, v203
	v_add_u32_e32 v30, 0x14000, v203
	ds_read_b128 v[2:5], v14
	ds_read_b128 v[6:9], v14 offset:1024
	ds_read_b128 v[10:13], v14 offset:2048
	ds_read_b128 v[14:17], v14 offset:3072
	ds_read_b128 v[18:21], v30
	ds_read_b128 v[22:25], v30 offset:1024
	ds_read_b128 v[26:29], v30 offset:2048
	ds_read_b128 v[30:33], v30 offset:3072
	s_lshl_b32 s48, s95, 7
	s_add_i32 s49, s48, 0x100
	s_add_i32 s50, s49, s92
	s_and_b64 s[46:47], s[10:11], exec
	v_add_u32_e32 v34, s49, v209
	s_cselect_b32 s47, s93, s50
	v_cndmask_b32_e64 v211, v34, v210, s[10:11]
	s_or_b32 s46, s47, 0x80
	v_add_u32_e32 v212, 0x80, v211
	s_add_i32 s48, s48, s94
	s_mov_b32 m0, s77
	ds_read_b128 v[34:37], v204
	ds_read_b128 v[38:41], v204 offset:1024
	ds_read_b128 v[42:45], v204 offset:2048
	ds_read_b128 v[46:49], v204 offset:3072
	ds_read_b128 v[50:53], v204 offset:4096
	ds_read_b128 v[54:57], v204 offset:5120
	ds_read_b128 v[58:61], v204 offset:6144
	ds_read_b128 v[62:65], v204 offset:7168
	buffer_load_dwordx4 v194, s[12:15], s48 offen lds
	s_mov_b32 m0, s78
	s_nop 0
	buffer_load_dwordx4 v195, s[12:15], s48 offen lds
	s_waitcnt vmcnt(8)
	s_waitcnt lgkmcnt(0)
	s_barrier
	s_setprio 1
	s_waitcnt lgkmcnt(6)
	v_mfma_f32_16x16x128_f8f6f4 v[190:193], v[2:9], v[34:41], v[190:193]
	v_mfma_f32_16x16x128_f8f6f4 v[186:189], v[10:17], v[34:41], v[186:189]
	s_waitcnt lgkmcnt(4)
	v_mfma_f32_16x16x128_f8f6f4 v[174:177], v[2:9], v[42:49], v[174:177]
	v_mfma_f32_16x16x128_f8f6f4 v[170:173], v[10:17], v[42:49], v[170:173]
	s_waitcnt lgkmcnt(2)
	v_mfma_f32_16x16x128_f8f6f4 v[158:161], v[2:9], v[50:57], v[158:161]
	v_mfma_f32_16x16x128_f8f6f4 v[154:157], v[10:17], v[50:57], v[154:157]
	s_waitcnt lgkmcnt(0)
	v_mfma_f32_16x16x128_f8f6f4 v[142:145], v[2:9], v[58:65], v[142:145]
	v_mfma_f32_16x16x128_f8f6f4 v[138:141], v[10:17], v[58:65], v[138:141]
	s_setprio 0
	s_setprio 1
	v_mfma_f32_16x16x128_f8f6f4 v[182:185], v[18:25], v[34:41], v[182:185]
	v_mfma_f32_16x16x128_f8f6f4 v[178:181], v[26:33], v[34:41], v[178:181]
	v_mfma_f32_16x16x128_f8f6f4 v[166:169], v[18:25], v[42:49], v[166:169]
	v_mfma_f32_16x16x128_f8f6f4 v[162:165], v[26:33], v[42:49], v[162:165]
	v_mfma_f32_16x16x128_f8f6f4 v[150:153], v[18:25], v[50:57], v[150:153]
	v_mfma_f32_16x16x128_f8f6f4 v[146:149], v[26:33], v[50:57], v[146:149]
	v_mfma_f32_16x16x128_f8f6f4 v[134:137], v[18:25], v[58:65], v[134:137]
	v_mfma_f32_16x16x128_f8f6f4 v[130:133], v[26:33], v[58:65], v[130:133]
	s_setprio 0
	s_barrier
	ds_read_b128 v[34:37], v204 offset:16384
	ds_read_b128 v[38:41], v204 offset:17408
	ds_read_b128 v[42:45], v204 offset:18432
	ds_read_b128 v[46:49], v204 offset:19456
	ds_read_b128 v[50:53], v204 offset:20480
	ds_read_b128 v[54:57], v204 offset:21504
	ds_read_b128 v[58:61], v204 offset:22528
	ds_read_b128 v[62:65], v204 offset:23552
	s_mov_b64 s[10:11], exec
	s_mov_b32 m0, s60
	v_readfirstlane_b32 s48, v211
	s_nop 4
	buffer_load_dwordx4 v196, s[16:19], s48 offen lds
	s_mov_b64 exec, s[10:11]
	s_mov_b64 s[10:11], exec
	s_mov_b32 m0, s61
	s_nop 0
	buffer_load_dwordx4 v197, s[16:19], s48 offen lds
	s_mov_b64 exec, s[10:11]
	v_add_u32_e32 v213, 0x20000, v211
	s_mov_b64 s[10:11], exec
	s_mov_b32 m0, s62
	v_readfirstlane_b32 s48, v213
	s_nop 4
	buffer_load_dwordx4 v196, s[16:19], s48 offen lds
	s_mov_b64 exec, s[10:11]
	s_mov_b64 s[10:11], exec
	s_mov_b32 m0, s63
	s_nop 0
	buffer_load_dwordx4 v197, s[16:19], s48 offen lds
	s_mov_b64 exec, s[10:11]
	s_mov_b32 m0, s59
	s_nop 0
	buffer_load_dwordx4 v194, s[12:15], s47 offen lds
	s_mov_b32 m0, s64
	s_nop 0
	buffer_load_dwordx4 v195, s[12:15], s47 offen lds
	s_waitcnt vmcnt(8)
	s_waitcnt lgkmcnt(0)
	s_barrier
	s_setprio 1
	s_waitcnt lgkmcnt(6)
	v_mfma_f32_16x16x128_f8f6f4 v[126:129], v[2:9], v[34:41], v[126:129]
	v_mfma_f32_16x16x128_f8f6f4 v[122:125], v[10:17], v[34:41], v[122:125]
	s_waitcnt lgkmcnt(4)
	v_mfma_f32_16x16x128_f8f6f4 v[110:113], v[2:9], v[42:49], v[110:113]
	v_mfma_f32_16x16x128_f8f6f4 v[106:109], v[10:17], v[42:49], v[106:109]
	s_waitcnt lgkmcnt(2)
	v_mfma_f32_16x16x128_f8f6f4 v[94:97], v[2:9], v[50:57], v[94:97]
	v_mfma_f32_16x16x128_f8f6f4 v[90:93], v[10:17], v[50:57], v[90:93]
	s_waitcnt lgkmcnt(0)
	v_mfma_f32_16x16x128_f8f6f4 v[78:81], v[2:9], v[58:65], v[78:81]
	v_mfma_f32_16x16x128_f8f6f4 v[74:77], v[10:17], v[58:65], v[74:77]
	s_setprio 0
	s_setprio 1
	v_mfma_f32_16x16x128_f8f6f4 v[118:121], v[18:25], v[34:41], v[118:121]
	v_mfma_f32_16x16x128_f8f6f4 v[114:117], v[26:33], v[34:41], v[114:117]
	v_mfma_f32_16x16x128_f8f6f4 v[102:105], v[18:25], v[42:49], v[102:105]
	v_mfma_f32_16x16x128_f8f6f4 v[98:101], v[26:33], v[42:49], v[98:101]
	v_mfma_f32_16x16x128_f8f6f4 v[86:89], v[18:25], v[50:57], v[86:89]
	v_mfma_f32_16x16x128_f8f6f4 v[82:85], v[26:33], v[50:57], v[82:85]
	v_mfma_f32_16x16x128_f8f6f4 v[70:73], v[18:25], v[58:65], v[70:73]
	v_mfma_f32_16x16x128_f8f6f4 v[66:69], v[26:33], v[58:65], v[66:69]
	s_setprio 0
	s_barrier
	v_add_u32_e32 v14, 0x18000, v203
	v_add_u32_e32 v30, 0x1c000, v203
	ds_read_b128 v[2:5], v14
	ds_read_b128 v[6:9], v14 offset:1024
	ds_read_b128 v[10:13], v14 offset:2048
	ds_read_b128 v[14:17], v14 offset:3072
	ds_read_b128 v[18:21], v30
	ds_read_b128 v[22:25], v30 offset:1024
	ds_read_b128 v[26:29], v30 offset:2048
	ds_read_b128 v[30:33], v30 offset:3072
	s_add_i32 s47, s47, 0x20000
	s_mov_b32 m0, s65
	ds_read_b128 v[34:37], v204 offset:32768
	ds_read_b128 v[38:41], v204 offset:33792
	ds_read_b128 v[42:45], v204 offset:34816
	ds_read_b128 v[46:49], v204 offset:35840
	ds_read_b128 v[50:53], v204 offset:36864
	ds_read_b128 v[54:57], v204 offset:37888
	ds_read_b128 v[58:61], v204 offset:38912
	ds_read_b128 v[62:65], v204 offset:39936
	buffer_load_dwordx4 v194, s[12:15], s47 offen lds
	s_mov_b32 m0, s66
	s_nop 0
	buffer_load_dwordx4 v195, s[12:15], s47 offen lds
	s_waitcnt vmcnt(8)
	s_waitcnt lgkmcnt(0)
	s_barrier
	s_setprio 1
	s_waitcnt lgkmcnt(6)
	v_mfma_f32_16x16x128_f8f6f4 v[190:193], v[2:9], v[34:41], v[190:193]
	v_mfma_f32_16x16x128_f8f6f4 v[186:189], v[10:17], v[34:41], v[186:189]
	s_waitcnt lgkmcnt(4)
	v_mfma_f32_16x16x128_f8f6f4 v[174:177], v[2:9], v[42:49], v[174:177]
	v_mfma_f32_16x16x128_f8f6f4 v[170:173], v[10:17], v[42:49], v[170:173]
	s_waitcnt lgkmcnt(2)
	v_mfma_f32_16x16x128_f8f6f4 v[158:161], v[2:9], v[50:57], v[158:161]
	v_mfma_f32_16x16x128_f8f6f4 v[154:157], v[10:17], v[50:57], v[154:157]
	s_waitcnt lgkmcnt(0)
	v_mfma_f32_16x16x128_f8f6f4 v[142:145], v[2:9], v[58:65], v[142:145]
	v_mfma_f32_16x16x128_f8f6f4 v[138:141], v[10:17], v[58:65], v[138:141]
	s_setprio 0
	s_setprio 1
	v_mfma_f32_16x16x128_f8f6f4 v[182:185], v[18:25], v[34:41], v[182:185]
	v_mfma_f32_16x16x128_f8f6f4 v[178:181], v[26:33], v[34:41], v[178:181]
	v_mfma_f32_16x16x128_f8f6f4 v[166:169], v[18:25], v[42:49], v[166:169]
	v_mfma_f32_16x16x128_f8f6f4 v[162:165], v[26:33], v[42:49], v[162:165]
	v_mfma_f32_16x16x128_f8f6f4 v[150:153], v[18:25], v[50:57], v[150:153]
	v_mfma_f32_16x16x128_f8f6f4 v[146:149], v[26:33], v[50:57], v[146:149]
	v_mfma_f32_16x16x128_f8f6f4 v[134:137], v[18:25], v[58:65], v[134:137]
	v_mfma_f32_16x16x128_f8f6f4 v[130:133], v[26:33], v[58:65], v[130:133]
	s_setprio 0
	s_barrier
	ds_read_b128 v[34:37], v204 offset:49152
	ds_read_b128 v[38:41], v204 offset:50176
	ds_read_b128 v[42:45], v204 offset:51200
	ds_read_b128 v[46:49], v204 offset:52224
	ds_read_b128 v[50:53], v204 offset:53248
	ds_read_b128 v[54:57], v204 offset:54272
	ds_read_b128 v[58:61], v204 offset:55296
	ds_read_b128 v[62:65], v204 offset:56320
	s_mov_b64 s[10:11], exec
	s_mov_b32 m0, s70
	v_readfirstlane_b32 s47, v212
	s_nop 4
	buffer_load_dwordx4 v196, s[16:19], s47 offen lds
	s_mov_b64 exec, s[10:11]
	s_mov_b64 s[10:11], exec
	s_mov_b32 m0, s71
	s_nop 0
	buffer_load_dwordx4 v197, s[16:19], s47 offen lds
	s_mov_b64 exec, s[10:11]
	v_add_u32_e32 v211, 0x20080, v211
	s_mov_b64 s[10:11], exec
	s_mov_b32 m0, s74
	v_readfirstlane_b32 s47, v211
	s_nop 4
	buffer_load_dwordx4 v196, s[16:19], s47 offen lds
	s_mov_b64 exec, s[10:11]
	s_mov_b64 s[10:11], exec
	s_mov_b32 m0, s75
	s_nop 0
	buffer_load_dwordx4 v197, s[16:19], s47 offen lds
	s_mov_b64 exec, s[10:11]
	s_mov_b32 m0, s72
	s_nop 0
	buffer_load_dwordx4 v194, s[12:15], s46 offen lds
	s_mov_b32 m0, s73
	s_nop 0
	buffer_load_dwordx4 v195, s[12:15], s46 offen lds
	s_waitcnt vmcnt(8)
	s_waitcnt lgkmcnt(0)
	s_barrier
	s_setprio 1
	s_waitcnt lgkmcnt(6)
	v_mfma_f32_16x16x128_f8f6f4 v[126:129], v[2:9], v[34:41], v[126:129]
	v_mfma_f32_16x16x128_f8f6f4 v[122:125], v[10:17], v[34:41], v[122:125]
	s_waitcnt lgkmcnt(4)
	v_mfma_f32_16x16x128_f8f6f4 v[110:113], v[2:9], v[42:49], v[110:113]
	v_mfma_f32_16x16x128_f8f6f4 v[106:109], v[10:17], v[42:49], v[106:109]
	s_waitcnt lgkmcnt(2)
	v_mfma_f32_16x16x128_f8f6f4 v[94:97], v[2:9], v[50:57], v[94:97]
	v_mfma_f32_16x16x128_f8f6f4 v[90:93], v[10:17], v[50:57], v[90:93]
	s_waitcnt lgkmcnt(0)
	v_mfma_f32_16x16x128_f8f6f4 v[78:81], v[2:9], v[58:65], v[78:81]
	v_mfma_f32_16x16x128_f8f6f4 v[74:77], v[10:17], v[58:65], v[74:77]
	s_setprio 0
	s_setprio 1
	v_mfma_f32_16x16x128_f8f6f4 v[118:121], v[18:25], v[34:41], v[118:121]
	v_mfma_f32_16x16x128_f8f6f4 v[114:117], v[26:33], v[34:41], v[114:117]
	v_mfma_f32_16x16x128_f8f6f4 v[102:105], v[18:25], v[42:49], v[102:105]
	v_mfma_f32_16x16x128_f8f6f4 v[98:101], v[26:33], v[42:49], v[98:101]
	v_mfma_f32_16x16x128_f8f6f4 v[86:89], v[18:25], v[50:57], v[86:89]
	v_mfma_f32_16x16x128_f8f6f4 v[82:85], v[26:33], v[50:57], v[82:85]
	v_mfma_f32_16x16x128_f8f6f4 v[70:73], v[18:25], v[58:65], v[70:73]
	v_mfma_f32_16x16x128_f8f6f4 v[66:69], v[26:33], v[58:65], v[66:69]
	s_setprio 0
	s_barrier
	s_add_i32 s95, s95, 2
	s_cmp_ge_i32 s95, s67
	s_cbranch_scc0 .LBB0_1927

.LBB0_3327:
	s_or_b64 exec, exec, s[4:5]
	s_add_u32 s54, s40, 0x1a000
	s_addc_u32 s55, s41, 0
	s_add_u32 s24, s0, 0xf8
	s_addc_u32 s25, s1, 0
	s_add_i32 s4, 0, 0x20080
	v_mov_b32_e32 v1, s4
	s_waitcnt lgkmcnt(0)
	s_barrier
	ds_read_b32 v2, v1
	s_load_dword s33, s[0:1], 0xf8
	s_add_u32 s26, s40, 0x300000
	s_addc_u32 s27, s41, 0
	s_add_u32 s12, s40, 0x36600000
	s_waitcnt lgkmcnt(0)
	v_readfirstlane_b32 s35, v2
	v_mov_b32 v2, v0
	ds_read_b32 v1, v1
	s_addc_u32 s4, s41, 0
	s_and_b32 s13, s4, 0xffff
	s_mov_b32 s15, 0x20000
	s_brev_b32 s14, -2
	s_waitcnt lgkmcnt(0)
	v_lshlrev_b32_e32 v1, 3, v1
	v_cmp_ge_i32_e32 vcc, s2, v1
	v_readfirstlane_b32 s6, v2
	s_cbranch_vccnz .LBB0_3386
	v_ashrrev_i32_e32 v1, 31, v2
	v_lshrrev_b32_e32 v1, 26, v1
	v_add_u32_e32 v1, v2, v1
	v_ashrrev_i32_e32 v12, 6, v1
	v_bfe_i32 v1, v2, 27, 1
	v_lshlrev_b32_e32 v3, 4, v2
	v_lshrrev_b32_e32 v1, 22, v1
	v_add_u32_e32 v1, v3, v1
	v_and_b32_e32 v1, 0xfffffc00, v1
	v_sub_u32_e32 v1, v3, v1
	v_lshrrev_b32_e32 v4, 4, v1
	v_bitop3_b32 v13, v4, v1, 32 bitop3:0x6c
	v_ashrrev_i32_e32 v1, 31, v1
	v_lshrrev_b32_e32 v1, 26, v1
	v_lshlrev_b32_e32 v4, 3, v12
	v_add_u32_e32 v1, v13, v1
	v_and_b32_e32 v4, -16, v4
	v_ashrrev_i32_e32 v14, 6, v1
	v_add_u32_e32 v3, 0x2000, v3
	v_add_u32_e32 v1, v14, v4
	v_ashrrev_i32_e32 v4, 31, v3
	v_lshrrev_b32_e32 v4, 22, v4
	v_add_u32_e32 v4, v3, v4
	v_ashrrev_i32_e32 v15, 10, v4
	v_mul_i32_i24_e32 v4, 0x400, v15
	v_sub_u32_e32 v3, v3, v4
	s_add_u32 s16, s40, 0xdc00000
	v_lshrrev_b32_e32 v4, 4, v3
	s_addc_u32 s4, s41, 0
	v_bitop3_b32 v3, v4, v3, 32 bitop3:0x6c
	v_lshlrev_b32_e32 v4, 3, v15
	s_add_u32 s20, s40, 0x4dd00000
	v_and_b32_e32 v16, -16, v4
	v_ashrrev_i32_e32 v4, 31, v3
	s_addc_u32 s5, s41, 0
	v_lshrrev_b32_e32 v4, 26, v4
	s_add_i32 s7, 0, 0x20044
	v_add_u32_e32 v17, v3, v4
	v_mov_b32_e32 v4, s7
	ds_read2_b32 v[4:5], v4 offset1:1
	s_add_i32 s7, 0, 0x2004c
	v_mov_b32_e32 v6, s7
	s_add_i32 s7, 0, 0x20054
	v_mov_b32_e32 v8, s7
	s_add_i32 s7, 0, 0x2005c
	v_mov_b32_e32 v10, s7
	s_ashr_i32 s46, s2, 3
	ds_read2_b32 v[6:7], v6 offset1:1
	ds_read2_b32 v[8:9], v8 offset1:1
	ds_read2_b32 v[10:11], v10 offset1:1
	s_waitcnt lgkmcnt(3)
	v_cmp_ge_i32_e32 vcc, s46, v4
	s_add_i32 s7, 0, 0x20064
	v_add_u32_e32 v197, 0x80, v1
	v_cndmask_b32_e64 v4, 0, 1, vcc
	v_cmp_lt_i32_e32 vcc, s46, v5
	s_mov_b32 s8, 0x1fffe0
	s_and_b32 s17, s4, 0xffff
	v_cndmask_b32_e32 v4, 2, v4, vcc
	s_waitcnt lgkmcnt(2)
	v_cmp_lt_i32_e32 vcc, s46, v6
	s_and_b32 s38, s2, 7
	s_and_b32 s21, s5, 0xffff
	v_cndmask_b32_e32 v4, 3, v4, vcc
	v_cmp_lt_i32_e32 vcc, s46, v7
	s_lshl_b32 s5, s38, 19
	s_mov_b32 s22, s14
	v_cndmask_b32_e32 v4, 4, v4, vcc
	s_waitcnt lgkmcnt(1)
	v_cmp_lt_i32_e32 vcc, s46, v8
	s_mov_b32 s23, s15
	s_mov_b32 s18, s14
	v_cndmask_b32_e32 v4, 5, v4, vcc
	v_cmp_lt_i32_e32 vcc, s46, v9
	s_mov_b32 s19, s15
	s_nop 0
	v_cndmask_b32_e32 v4, 6, v4, vcc
	s_waitcnt lgkmcnt(0)
	v_cmp_lt_i32_e32 vcc, s46, v10
	s_nop 1
	v_cndmask_b32_e32 v4, 7, v4, vcc
	v_cmp_lt_i32_e32 vcc, s46, v11
	s_nop 1
	v_cndmask_b32_e32 v10, 8, v4, vcc
	v_mov_b32_e32 v4, s7
	ds_read2_b32 v[4:5], v4 offset1:1
	s_add_i32 s7, 0, 0x2006c
	v_mov_b32_e32 v6, s7
	s_add_i32 s7, 0, 0x20074
	v_mov_b32_e32 v8, s7
	s_add_i32 s7, 0, 0x2007c
	v_mov_b32_e32 v11, s7
	ds_read2_b32 v[6:7], v6 offset1:1
	ds_read2_b32 v[8:9], v8 offset1:1
	ds_read_b32 v11, v11
	s_waitcnt lgkmcnt(3)
	v_cmp_lt_i32_e32 vcc, s46, v4
	s_movk_i32 s7, 0x4200
	s_nop 0
	v_cndmask_b32_e32 v4, 9, v10, vcc
	v_cmp_lt_i32_e32 vcc, s46, v5
	v_ashrrev_i32_e32 v10, 6, v17
	v_add_u32_e32 v196, v10, v16
	v_cndmask_b32_e32 v4, 10, v4, vcc
	s_waitcnt lgkmcnt(2)
	v_cmp_lt_i32_e32 vcc, s46, v6
	v_add_u32_e32 v198, 0x80, v196
	s_nop 0
	v_cndmask_b32_e32 v4, 11, v4, vcc
	v_cmp_lt_i32_e32 vcc, s46, v7
	s_nop 1
	v_cndmask_b32_e32 v4, 12, v4, vcc
	s_waitcnt lgkmcnt(1)
	v_cmp_lt_i32_e32 vcc, s46, v8
	s_nop 1
	v_cndmask_b32_e32 v4, 13, v4, vcc
	v_cmp_lt_i32_e32 vcc, s46, v9
	s_nop 1
	v_cndmask_b32_e32 v4, 14, v4, vcc
	s_waitcnt lgkmcnt(0)
	v_cmp_lt_i32_e32 vcc, s46, v11
	s_nop 1
	v_cndmask_b32_e32 v194, 15, v4, vcc
	v_lshlrev_b32_e32 v4, 2, v194
	v_add_u32_e32 v4, 0, v4
	v_add_u32_e32 v4, 0x20000, v4
	ds_read2_b32 v[4:5], v4 offset1:16
	v_mul_lo_u32 v11, v194, s7
	s_ashr_i32 s7, s6, 8
	s_waitcnt lgkmcnt(0)
	v_sub_u32_e32 v5, s46, v5
	v_lshlrev_b32_e32 v16, 8, v5
	v_add_u32_e32 v5, v16, v1
	v_add_u32_e32 v18, -1, v4
	v_min_i32_e32 v4, v5, v18
	v_add_u32_e32 v6, v16, v197
	v_add_u32_e32 v8, v16, v196
	v_add_u32_e32 v4, v4, v11
	v_min_i32_e32 v6, v6, v18
	v_min_i32_e32 v8, v8, v18
	v_ashrrev_i32_e32 v5, 31, v4
	v_add_u32_e32 v6, v6, v11
	v_add_u32_e32 v8, v8, v11
	v_lshl_add_u64 v[4:5], v[4:5], 2, s[26:27]
	v_ashrrev_i32_e32 v7, 31, v6
	v_ashrrev_i32_e32 v9, 31, v8
	v_lshl_add_u64 v[6:7], v[6:7], 2, s[26:27]
	v_lshl_add_u64 v[8:9], v[8:9], 2, s[26:27]
	global_load_dword v19, v[4:5], off
	global_load_dword v20, v[6:7], off
	global_load_dword v21, v[8:9], off
	v_add_u32_e32 v4, v16, v198
	v_min_i32_e32 v4, v4, v18
	v_add_u32_e32 v4, v4, v11
	v_ashrrev_i32_e32 v5, 31, v4
	v_lshl_add_u64 v[4:5], v[4:5], 2, s[26:27]
	global_load_dword v4, v[4:5], off
	v_mul_i32_i24_e32 v6, 64, v14
	v_sub_u32_e32 v6, v13, v6
	v_mov_b32_e32 v7, 1
	v_lshlrev_b32_e32 v5, 5, v12
	v_ashrrev_i16_sdwa v6, v7, sext(v6) dst_sel:DWORD dst_unused:UNUSED_PAD src0_sel:DWORD src1_sel:BYTE_0
	v_and_b32_e32 v5, 32, v5
	v_bfe_i32 v6, v6, 0, 16
	v_add_lshl_u32 v199, v5, v6, 1
	v_and_b32_e32 v6, 0xc0, v17
	v_sub_u32_e32 v3, v3, v6
	v_lshlrev_b32_e32 v5, 5, v15
	v_ashrrev_i16_sdwa v3, v7, sext(v3) dst_sel:DWORD dst_unused:UNUSED_PAD src0_sel:DWORD src1_sel:BYTE_0
	v_and_b32_e32 v5, 32, v5
	v_bfe_i32 v3, v3, 0, 16
	v_add_lshl_u32 v201, v5, v3, 1
	v_lshlrev_b32_e32 v8, 1, v1
	v_lshrrev_b32_e32 v9, 2, v1
	v_and_b32_e32 v11, 3, v14
	v_and_b32_e32 v8, 24, v8
	v_and_b32_e32 v9, 4, v9
	v_and_or_b32 v11, v1, s8, v11
	v_or3_b32 v8, v11, v9, v8
	v_lshl_add_u32 v200, v8, 11, v199
	v_and_b32_e32 v8, 3, v10
	v_lshlrev_b32_e32 v6, 1, v196
	v_lshrrev_b32_e32 v7, 2, v196
	v_and_or_b32 v8, v196, s8, v8
	s_ashr_i32 s8, s6, 6
	v_and_b32_e32 v6, 24, v6
	v_and_b32_e32 v7, 4, v7
	s_lshl_b32 s4, s8, 10
	v_or3_b32 v6, v8, v7, v6
	s_add_i32 s47, s4, 0
	v_lshl_add_u32 v202, v6, 11, v201
	s_add_i32 s48, s47, 0x10000
	s_mov_b32 m0, s48
	s_waitcnt vmcnt(3)
	v_lshlrev_b32_e32 v3, 10, v19
	v_and_b32_e32 v3, 0xfffff800, v3
	v_add_u32_e32 v195, v3, v199
	s_waitcnt vmcnt(2)
	v_lshlrev_b32_e32 v3, 10, v20
	v_and_b32_e32 v3, 0xfffff800, v3
	v_add_u32_e32 v218, v3, v199
	s_waitcnt vmcnt(1)
	v_lshlrev_b32_e32 v3, 10, v21
	v_and_b32_e32 v3, 0xfffff800, v3
	v_add_u32_e32 v217, v3, v201
	s_waitcnt vmcnt(0)
	v_lshlrev_b32_e32 v3, 10, v4
	v_and_b32_e32 v3, 0xfffff800, v3
	v_add_u32_e32 v219, v3, v201
	v_lshlrev_b32_e32 v3, 22, v194
	v_or_b32_e32 v220, s5, v3
	s_mov_b64 s[4:5], exec
	v_readfirstlane_b32 s9, v220
	s_nop 4
	buffer_load_dwordx4 v200, s[16:19], s9 offen lds
	s_mov_b64 exec, s[4:5]
	s_add_i32 s49, s47, 0x12000
	s_mov_b64 s[4:5], exec
	s_mov_b32 m0, s49
	s_nop 0
	buffer_load_dwordx4 v202, s[16:19], s9 offen lds
	s_mov_b64 exec, s[4:5]
	s_add_i32 s50, s47, 0x14000
	v_or_b32_e32 v3, 0x40000, v220
	s_mov_b64 s[4:5], exec
	s_mov_b32 m0, s50
	v_readfirstlane_b32 s9, v3
	s_nop 4
	buffer_load_dwordx4 v200, s[16:19], s9 offen lds
	s_mov_b64 exec, s[4:5]
	s_add_i32 s51, s47, 0x16000
	s_mov_b64 s[4:5], exec
	s_mov_b32 m0, s51
	s_nop 0
	buffer_load_dwordx4 v202, s[16:19], s9 offen lds
	s_mov_b64 exec, s[4:5]
	s_mov_b32 m0, s47
	s_add_i32 s52, s47, 0x2000
	buffer_load_dwordx4 v195, s[20:23], 0 offen lds
	s_mov_b32 m0, s52
	s_add_i32 s53, s47, 0x4000
	buffer_load_dwordx4 v217, s[20:23], 0 offen lds
	s_mov_b32 m0, s53
	s_add_i32 s56, s47, 0x6000
	buffer_load_dwordx4 v218, s[20:23], 0 offen lds
	s_mov_b32 m0, s56
	s_cmp_eq_u32 s7, 1
	buffer_load_dwordx4 v219, s[20:23], 0 offen lds
	s_cselect_b64 s[10:11], -1, 0
	s_cmp_lg_u32 s7, 1
	s_cbranch_scc1 .LBB0_3338
	s_barrier
.LBB0_3338:
	v_and_b32_e32 v203, 15, v2
	s_add_u32 s28, s40, 0xc040
	v_bfe_u32 v204, v2, 4, 2
	v_lshlrev_b32_e32 v3, 6, v203
	v_lshlrev_b32_e32 v2, 2, v2
	s_addc_u32 s29, s41, 0
	v_lshl_or_b32 v3, v204, 4, v3
	s_lshl_b32 s4, s7, 13
	v_and_b32_e32 v4, 32, v2
	v_bitop3_b32 v2, v3, s4, v4 bitop3:0xde
	s_lshl_b32 s4, s8, 5
	s_and_b32 s8, s4, 0x60
	s_waitcnt vmcnt(2)
	s_lshl_b32 s4, s8, 7
	v_bitop3_b32 v3, v3, s4, v4 bitop3:0xde
	s_add_i32 s57, s47, 0x18000
	s_movk_i32 s9, 0x80
	v_or_b32_e32 v4, 0x80, v220
	s_mov_b32 s18, s14
	s_mov_b32 s19, s15
	s_mov_b64 s[4:5], exec
	s_barrier
	s_mov_b32 m0, s57
	v_readfirstlane_b32 s22, v4
	s_nop 4
	buffer_load_dwordx4 v200, s[16:19], s22 offen lds
	s_mov_b64 exec, s[4:5]
	s_add_i32 s58, s47, 0x1a000
	s_mov_b64 s[4:5], exec
	s_mov_b32 m0, s58
	s_nop 0
	buffer_load_dwordx4 v202, s[16:19], s22 offen lds
	s_mov_b64 exec, s[4:5]
	s_add_i32 s59, s47, 0x8000
	s_mov_b32 s22, s14
	s_mov_b32 s23, s15
	s_mov_b32 m0, s59
	s_add_i32 s60, s47, 0xa000
	buffer_load_dwordx4 v195, s[20:23], s9 offen lds
	s_mov_b32 m0, s60
	s_add_i32 s61, s47, 0x1c000
	buffer_load_dwordx4 v217, s[20:23], s9 offen lds
	v_or_b32_e32 v4, 0x40080, v220
	s_mov_b64 s[4:5], exec
	s_mov_b32 m0, s61
	v_readfirstlane_b32 s9, v4
	s_nop 4
	buffer_load_dwordx4 v200, s[16:19], s9 offen lds
	s_mov_b64 exec, s[4:5]
	s_add_i32 s62, s47, 0x1e000
	s_mov_b64 s[4:5], exec
	s_mov_b32 m0, s62
	s_nop 0
	buffer_load_dwordx4 v202, s[16:19], s9 offen lds
	s_mov_b64 exec, s[4:5]
	s_add_i32 s63, s47, 0xc000
	s_cmpk_lt_u32 s6, 0x100
	s_waitcnt vmcnt(6)
	s_cselect_b64 s[30:31], -1, 0
	s_lshl_b32 s6, s7, 16
	v_and_b32_e32 v4, 63, v0
	s_or_b32 s66, s8, s6
	s_add_i32 s6, 0, 0x20080
	v_add_u32_e32 v206, 0, v3
	s_mov_b32 s64, 0
	v_cmp_eq_u32_e64 s[4:5], 0, v4
	s_add_i32 s65, s47, 0xe000
	v_mov_b32_e32 v205, s6
	s_add_i32 s67, 0, 0x20044
	s_add_i32 s68, 0, 0x2004c
	s_add_i32 s69, 0, 0x20054
	s_add_i32 s70, 0, 0x2005c
	s_add_i32 s71, 0, 0x20064
	s_add_i32 s72, 0, 0x2006c
	s_add_i32 s73, 0, 0x20074
	s_add_i32 s74, 0, 0x2007c
	s_movk_i32 s75, 0x4200
	v_add_u32_e32 v207, 0x10000, v206
	v_add_u32_e32 v208, 0x14000, v206
	v_add_u32_e32 v209, 0, v2
	s_mov_b32 s22, s14
	s_mov_b32 s23, s15
	s_mov_b32 s18, s14
	s_mov_b32 s19, s15
	v_mov_b32_e32 v210, 0
	s_brev_b32 s34, 60
	s_barrier
	s_branch .LBB0_3349

.LBB0_3406:
	s_or_b64 exec, exec, s[6:7]
	v_bfe_i32 v5, v2, 27, 1
	v_lshlrev_b32_e32 v3, 4, v2
	v_lshrrev_b32_e32 v5, 22, v5
	v_add_u32_e32 v5, v3, v5
	v_and_b32_e32 v5, 0xfffffc00, v5
	v_sub_u32_e32 v5, v3, v5
	v_lshrrev_b32_e32 v6, 4, v5
	v_bitop3_b32 v6, v6, v5, 32 bitop3:0x6c
	v_ashrrev_i32_e32 v5, 31, v5
	v_lshrrev_b32_e32 v5, 26, v5
	v_ashrrev_i32_e32 v4, 31, v2
	v_add_u32_e32 v5, v6, v5
	v_lshrrev_b32_e32 v4, 26, v4
	v_ashrrev_i32_e32 v5, 6, v5
	v_add_u32_e32 v4, v2, v4
	v_mul_i32_i24_e32 v8, 64, v5
	v_ashrrev_i32_e32 v4, 6, v4
	v_sub_u32_e32 v6, v6, v8
	v_mov_b32_e32 v8, 1
	v_lshlrev_b32_e32 v7, 3, v4
	v_lshlrev_b32_e32 v4, 5, v4
	v_ashrrev_i16_sdwa v6, v8, sext(v6) dst_sel:DWORD dst_unused:UNUSED_PAD src0_sel:DWORD src1_sel:BYTE_0
	v_and_b32_e32 v4, 32, v4
	v_bfe_i32 v6, v6, 0, 16
	v_add_u32_e32 v3, 0x2000, v3
	v_add_lshl_u32 v4, v4, v6, 1
	v_ashrrev_i32_e32 v6, 31, v3
	v_lshrrev_b32_e32 v6, 22, v6
	v_add_u32_e32 v6, v3, v6
	v_ashrrev_i32_e32 v6, 10, v6
	v_mul_i32_i24_e32 v9, 0x400, v6
	v_sub_u32_e32 v3, v3, v9
	v_lshrrev_b32_e32 v9, 4, v3
	v_bitop3_b32 v3, v9, v3, 32 bitop3:0x6c
	v_ashrrev_i32_e32 v10, 31, v3
	v_lshrrev_b32_e32 v10, 26, v10
	v_add_u32_e32 v10, v3, v10
	v_ashrrev_i32_e32 v11, 6, v10
	v_and_b32_e32 v10, 0xc0, v10
	v_sub_u32_e32 v3, v3, v10
	v_lshlrev_b32_e32 v9, 3, v6
	v_lshlrev_b32_e32 v6, 5, v6
	v_ashrrev_i16_sdwa v3, v8, sext(v3) dst_sel:DWORD dst_unused:UNUSED_PAD src0_sel:DWORD src1_sel:BYTE_0
	v_and_b32_e32 v7, -16, v7
	v_and_b32_e32 v6, 32, v6
	v_bfe_i32 v3, v3, 0, 16
	v_add_u32_e32 v7, v5, v7
	v_add_lshl_u32 v3, v6, v3, 1
	v_lshlrev_b32_e32 v6, 21, v208
	s_lshl_b32 s6, s58, 18
	v_add_u32_e32 v209, s6, v6
	v_lshlrev_b32_e32 v6, 1, v7
	v_lshrrev_b32_e32 v8, 2, v7
	v_and_b32_e32 v5, 3, v5
	s_mov_b32 s7, 0x3fffe0
	v_and_b32_e32 v9, -16, v9
	s_lshl_b32 s92, s34, 18
	v_and_b32_e32 v6, 24, v6
	v_and_b32_e32 v8, 4, v8
	v_and_or_b32 v5, v7, s7, v5
	v_add_u32_e32 v9, v11, v9
	s_add_u32 s16, s40, 0x1bc00000
	v_or3_b32 v5, v5, v8, v6
	v_lshl_add_u32 v194, v7, 10, v4
	s_addc_u32 s6, s41, 0
	v_lshl_add_u32 v196, v5, 10, v4
	v_lshlrev_b32_e32 v4, 1, v9
	v_lshrrev_b32_e32 v5, 2, v9
	v_and_b32_e32 v6, 3, v11
	s_ashr_i32 s9, s31, 6
	v_and_b32_e32 v4, 24, v4
	v_and_b32_e32 v5, 4, v5
	v_and_or_b32 v6, v9, s7, v6
	s_and_b32 s17, s6, 0xffff
	s_lshl_b32 s6, s9, 10
	s_barrier
	v_or3_b32 v4, v6, v5, v4
	s_add_i32 s59, s6, 0
	v_lshl_add_u32 v195, v9, 10, v3
	s_ashr_i32 s8, s31, 8
	v_lshl_add_u32 v197, v4, 10, v3
	s_mov_b32 s19, 0x20000
	s_brev_b32 s18, -2
	s_add_i32 s60, s59, 0x10000
	s_mov_b64 s[6:7], exec
	s_mov_b32 m0, s60
	v_readfirstlane_b32 s10, v209
	s_nop 4
	buffer_load_dwordx4 v196, s[16:19], s10 offen lds
	s_mov_b64 exec, s[6:7]
	s_add_i32 s61, s59, 0x12000
	s_mov_b64 s[6:7], exec
	s_mov_b32 m0, s61
	s_nop 0
	buffer_load_dwordx4 v197, s[16:19], s10 offen lds
	s_mov_b64 exec, s[6:7]
	s_add_i32 s62, s59, 0x14000
	v_or_b32_e32 v3, 0x20000, v209
	s_mov_b64 s[6:7], exec
	s_mov_b32 m0, s62
	v_readfirstlane_b32 s10, v3
	s_nop 4
	buffer_load_dwordx4 v196, s[16:19], s10 offen lds
	s_mov_b64 exec, s[6:7]
	s_add_i32 s63, s59, 0x16000
	s_mov_b64 s[6:7], exec
	s_mov_b32 m0, s63
	s_nop 0
	buffer_load_dwordx4 v197, s[16:19], s10 offen lds
	s_mov_b64 exec, s[6:7]
	s_mov_b32 m0, s59
	s_add_i32 s64, s59, 0x2000
	buffer_load_dwordx4 v194, s[12:15], s92 offen lds
	s_mov_b32 m0, s64
	s_add_i32 s65, s59, 0x4000
	buffer_load_dwordx4 v195, s[12:15], s92 offen lds
	s_or_b32 s6, s92, 0x20000
	s_mov_b32 m0, s65
	s_add_i32 s66, s59, 0x6000
	buffer_load_dwordx4 v194, s[12:15], s6 offen lds
	s_mov_b32 m0, s66
	s_cmp_eq_u32 s8, 1
	buffer_load_dwordx4 v195, s[12:15], s6 offen lds
	s_cselect_b64 s[20:21], -1, 0
	s_cmp_lg_u32 s8, 1
	s_cbranch_scc1 .LBB0_3416
	s_barrier
